# speedup vs baseline: 1.0033x; 1.0033x over previous
.LE_cdone1:
	s_waitcnt lgkmcnt(0)
	s_barrier
	v_mov_b32_e32 v252, 0x20800
	ds_read_b32 v200, v252
	ds_read_b32 v201, v252 offset:4
	ds_read_b32 v202, v252 offset:8
	s_waitcnt lgkmcnt(0)
	s_nop 1
	v_readfirstlane_b32 s31, v200
	v_readfirstlane_b32 s29, v201
	v_readfirstlane_b32 s30, v202
	s_nop 3
	s_barrier
	s_lshl_b32 s49, s29, 19
	s_lshl_b32 s64, s32, 13
	s_add_u32 s49, s49, s64
	s_mov_b32 s51, s64
	s_add_u32 s52, s51, 0x0
	s_add_u32 s53, s51, 0x1000
	s_add_u32 s54, s51, 0x8000
	s_add_u32 s55, s51, 0x9000
	s_add_u32 s56, s51, 0x10000
	s_add_u32 s57, s51, 0x11000
	s_add_u32 s58, s51, 0x18000
	s_add_u32 s59, s51, 0x19000
	s_lshl_b32 s64, s29, 8
	s_lshl_b32 s65, s30, 1
	s_add_u32 s64, s64, s65
	s_lshr_b32 s65, s32, 1
	s_add_u32 s64, s64, s65
	s_lshl_b32 s64, s64, 11
	s_and_b32 s65, s32, 1
	s_lshl_b32 s65, s65, 9
	s_add_u32 s50, s64, s65
	s_sub_u32 s60, s28, 1
	v_mov_b32_e32 v128, 0
	v_mov_b32_e32 v129, 0
	v_mov_b32_e32 v130, 0
	v_mov_b32_e32 v131, 0
	v_mov_b32_e32 v132, 0
	v_mov_b32_e32 v133, 0
	v_mov_b32_e32 v134, 0
	v_mov_b32_e32 v135, 0
	v_mov_b32_e32 v136, 0
	v_mov_b32_e32 v137, 0
	v_mov_b32_e32 v138, 0
	v_mov_b32_e32 v139, 0
	v_mov_b32_e32 v140, 0
	v_mov_b32_e32 v141, 0
	v_mov_b32_e32 v142, 0
	v_mov_b32_e32 v143, 0
	v_mov_b32_e32 v144, 0
	v_mov_b32_e32 v145, 0
	v_mov_b32_e32 v146, 0
	v_mov_b32_e32 v147, 0
	v_mov_b32_e32 v148, 0
	v_mov_b32_e32 v149, 0
	v_mov_b32_e32 v150, 0
	v_mov_b32_e32 v151, 0
	v_mov_b32_e32 v152, 0
	v_mov_b32_e32 v153, 0
	v_mov_b32_e32 v154, 0
	v_mov_b32_e32 v155, 0
	v_mov_b32_e32 v156, 0
	v_mov_b32_e32 v157, 0
	v_mov_b32_e32 v158, 0
	v_mov_b32_e32 v159, 0
	s_lshl_b32 s64, s30, 5
	s_lshl_b32 s65, s32, 3
	s_add_u32 s64, s64, s65
	v_lshlrev_b32_e32 v255, 2, v254
	v_add_u32_e32 v255, s64, v255
	v_lshlrev_b32_e32 v249, 3, v253
	v_lshl_add_u32 v249, v254, 2, v249
	v_lshlrev_b32_e32 v250, 12, v253
	v_lshl_add_u32 v250, v254, 4, v250
	v_lshrrev_b32_e32 v200, 3, v253
	v_and_b32_e32 v201, 7, v253
	v_lshl_add_u32 v202, v200, 10, v201
	v_add_u32_e32 v202, s64, v202
	v_lshl_add_u32 v202, v202, 1, v254
	v_lshlrev_b32_e32 v202, 2, v202
	global_load_dword v248, v202, s[14:15]
	v_mov_b32_e32 v203, 0xbfb8aa3b
	v_mov_b32_e32 v204, 0xc038aa3b
	v_cmp_eq_u32_e32 vcc, 2, v200
	s_nop 1
	v_cndmask_b32_e32 v203, v203, v204, vcc
	v_lshlrev_b32_e32 v205, 2, v255
	v_add_u32_e32 v206, 0x0, v205
	global_load_dwordx4 v[232:235], v206, s[16:17]
	v_add_u32_e32 v206, 0x1000, v205
	global_load_dwordx4 v[236:239], v206, s[16:17]
	v_add_u32_e32 v206, 0x2000, v205
	global_load_dwordx4 v[240:243], v206, s[16:17]
	v_add_u32_e32 v206, 0x3000, v205
	global_load_dwordx4 v[244:247], v206, s[16:17]
	s_waitcnt vmcnt(0)
	v_mul_f32_e32 v248, v203, v248
	s_mov_b32 s65, 0xbfb8aa3b
	v_mul_f32_e32 v232, s65, v232
	v_mul_f32_e32 v233, s65, v233
	v_mul_f32_e32 v234, s65, v234
	v_mul_f32_e32 v235, s65, v235
	s_mov_b32 s65, 0xbfb8aa3b
	v_mul_f32_e32 v236, s65, v236
	v_mul_f32_e32 v237, s65, v237
	v_mul_f32_e32 v238, s65, v238
	v_mul_f32_e32 v239, s65, v239
	s_mov_b32 s65, 0xc038aa3b
	v_mul_f32_e32 v240, s65, v240
	v_mul_f32_e32 v241, s65, v241
	v_mul_f32_e32 v242, s65, v242
	v_mul_f32_e32 v243, s65, v243
	s_mov_b32 s65, 0xbfb8aa3b
	v_mul_f32_e32 v244, s65, v244
	v_mul_f32_e32 v245, s65, v245
	v_mul_f32_e32 v246, s65, v246
	v_mul_f32_e32 v247, s65, v247
	s_lshl_b32 s65, s29, 20
	s_lshl_b32 s66, s64, 2
	s_add_u32 s65, s65, s66
	s_add_u32 s62, s26, s65
	s_addc_u32 s63, s27, 0
	s_waitcnt vmcnt(0)
	s_mov_b32 s33, 0
	s_lshl_b32 s64, s33, 11
	s_lshl_b32 s65, s29, 8
	s_add_u32 s64, s64, s65
	s_lshl_b32 s64, s64, 3
	s_add_u32 s42, s12, s64
	s_addc_u32 s43, s13, 0
	global_load_dword v228, v249, s[42:43] offset:0
	global_load_dword v229, v249, s[42:43] offset:256
	s_waitcnt vmcnt(0)
	v_mfma_f32_32x32x2_f32 v[0:15], v248, v228, v[232:247]
	v_mfma_f32_32x32x2_f32 v[16:31], v248, v229, v[232:247]
	s_nop 15
	s_nop 3
	s_lshl_b32 s64, s33, 11
	s_lshl_b32 s65, s29, 8
	s_add_u32 s64, s64, s65
	s_add_u32 s64, s64, 64
	s_lshl_b32 s64, s64, 3
	s_add_u32 s42, s12, s64
	s_addc_u32 s43, s13, 0
	global_load_dword v228, v249, s[42:43] offset:0
	global_load_dword v229, v249, s[42:43] offset:256
	s_waitcnt vmcnt(0)
	v_mfma_f32_32x32x2_f32 v[32:47], v248, v228, v[232:247]
	v_mfma_f32_32x32x2_f32 v[48:63], v248, v229, v[232:247]
	s_nop 15
	s_nop 3
	s_lshl_b32 s64, s33, 11
	s_lshl_b32 s65, s29, 8
	s_add_u32 s64, s64, s65
	s_add_u32 s64, s64, 128
	s_lshl_b32 s64, s64, 3
	s_add_u32 s42, s12, s64
	s_addc_u32 s43, s13, 0
	global_load_dword v228, v249, s[42:43] offset:0
	global_load_dword v229, v249, s[42:43] offset:256
	s_waitcnt vmcnt(0)
	v_mfma_f32_32x32x2_f32 v[64:79], v248, v228, v[232:247]
	v_mfma_f32_32x32x2_f32 v[80:95], v248, v229, v[232:247]
	s_nop 15
	s_nop 3
	s_lshl_b32 s64, s33, 11
	s_lshl_b32 s65, s29, 8
	s_add_u32 s64, s64, s65
	s_add_u32 s64, s64, 192
	s_lshl_b32 s64, s64, 3
	s_add_u32 s42, s12, s64
	s_addc_u32 s43, s13, 0
	global_load_dword v228, v249, s[42:43] offset:0
	global_load_dword v229, v249, s[42:43] offset:256
	s_waitcnt vmcnt(0)
	v_mfma_f32_32x32x2_f32 v[96:111], v248, v228, v[232:247]
	v_mfma_f32_32x32x2_f32 v[112:127], v248, v229, v[232:247]
	s_nop 15
	s_nop 3
	s_waitcnt vmcnt(0)
	s_waitcnt lgkmcnt(0)
	s_lshl_b32 s64, s30, 2
	s_add_u32 s64, s64, s32
	s_lshl_b32 s64, s64, 16
	s_add_u32 s44, s4, s64
	s_addc_u32 s45, s5, 0
	global_load_dwordx4 a[0:3], v192, s[44:45] offset:0
	global_load_dwordx4 a[4:7], v192, s[44:45] offset:1024
	global_load_dwordx4 a[8:11], v192, s[44:45] offset:2048
	global_load_dwordx4 a[12:15], v192, s[44:45] offset:3072
	s_add_u32 s44, s44, 0x1000
	s_addc_u32 s45, s45, 0
	global_load_dwordx4 a[16:19], v192, s[44:45] offset:0
	global_load_dwordx4 a[20:23], v192, s[44:45] offset:1024
	global_load_dwordx4 a[24:27], v192, s[44:45] offset:2048
	global_load_dwordx4 a[28:31], v192, s[44:45] offset:3072
	s_add_u32 s44, s44, 0x1000
	s_addc_u32 s45, s45, 0
	global_load_dwordx4 a[32:35], v192, s[44:45] offset:0
	global_load_dwordx4 a[36:39], v192, s[44:45] offset:1024
	global_load_dwordx4 a[40:43], v192, s[44:45] offset:2048
	global_load_dwordx4 a[44:47], v192, s[44:45] offset:3072
	s_add_u32 s44, s44, 0x1000
	s_addc_u32 s45, s45, 0
	global_load_dwordx4 a[48:51], v192, s[44:45] offset:0
	global_load_dwordx4 a[52:55], v192, s[44:45] offset:1024
	global_load_dwordx4 a[56:59], v192, s[44:45] offset:2048
	global_load_dwordx4 a[60:63], v192, s[44:45] offset:3072
	s_add_u32 s44, s44, 0x1000
	s_addc_u32 s45, s45, 0
	global_load_dwordx4 a[64:67], v192, s[44:45] offset:0
	global_load_dwordx4 a[68:71], v192, s[44:45] offset:1024
	global_load_dwordx4 a[72:75], v192, s[44:45] offset:2048
	global_load_dwordx4 a[76:79], v192, s[44:45] offset:3072
	s_add_u32 s44, s44, 0x1000
	s_addc_u32 s45, s45, 0
	global_load_dwordx4 a[80:83], v192, s[44:45] offset:0
	global_load_dwordx4 a[84:87], v192, s[44:45] offset:1024
	global_load_dwordx4 a[88:91], v192, s[44:45] offset:2048
	global_load_dwordx4 a[92:95], v192, s[44:45] offset:3072
	s_add_u32 s44, s44, 0x1000
	s_addc_u32 s45, s45, 0
	global_load_dwordx4 a[96:99], v192, s[44:45] offset:0
	global_load_dwordx4 a[100:103], v192, s[44:45] offset:1024
	global_load_dwordx4 a[104:107], v192, s[44:45] offset:2048
	global_load_dwordx4 a[108:111], v192, s[44:45] offset:3072
	s_add_u32 s44, s44, 0x1000
	s_addc_u32 s45, s45, 0
	global_load_dwordx4 a[112:115], v192, s[44:45] offset:0
	global_load_dwordx4 a[116:119], v192, s[44:45] offset:1024
	global_load_dwordx4 a[120:123], v192, s[44:45] offset:2048
	global_load_dwordx4 a[124:127], v192, s[44:45] offset:3072
	s_add_u32 s44, s44, 0x1000
	s_addc_u32 s45, s45, 0
	s_waitcnt vmcnt(16)
	global_load_dwordx4 a[128:131], v192, s[44:45] offset:0
	global_load_dwordx4 a[132:135], v192, s[44:45] offset:1024
	global_load_dwordx4 a[136:139], v192, s[44:45] offset:2048
	global_load_dwordx4 a[140:143], v192, s[44:45] offset:3072
	s_add_u32 s44, s44, 0x1000
	s_addc_u32 s45, s45, 0
	global_load_dwordx4 a[144:147], v192, s[44:45] offset:0
	global_load_dwordx4 a[148:151], v192, s[44:45] offset:1024
	global_load_dwordx4 a[152:155], v192, s[44:45] offset:2048
	global_load_dwordx4 a[156:159], v192, s[44:45] offset:3072
	s_add_u32 s44, s44, 0x1000
	s_addc_u32 s45, s45, 0
	global_load_dwordx4 a[160:163], v192, s[44:45] offset:0
	global_load_dwordx4 a[164:167], v192, s[44:45] offset:1024
	global_load_dwordx4 a[168:171], v192, s[44:45] offset:2048
	global_load_dwordx4 a[172:175], v192, s[44:45] offset:3072
	s_add_u32 s44, s44, 0x1000
	s_addc_u32 s45, s45, 0
	global_load_dwordx4 a[176:179], v192, s[44:45] offset:0
	global_load_dwordx4 a[180:183], v192, s[44:45] offset:1024
	global_load_dwordx4 a[184:187], v192, s[44:45] offset:2048
	global_load_dwordx4 a[188:191], v192, s[44:45] offset:3072
	s_add_u32 s44, s44, 0x1000
	s_addc_u32 s45, s45, 0
	global_load_dwordx4 a[192:195], v192, s[44:45] offset:0
	global_load_dwordx4 a[196:199], v192, s[44:45] offset:1024
	global_load_dwordx4 a[200:203], v192, s[44:45] offset:2048
	global_load_dwordx4 a[204:207], v192, s[44:45] offset:3072
	s_add_u32 s44, s44, 0x1000
	s_addc_u32 s45, s45, 0
	global_load_dwordx4 a[208:211], v192, s[44:45] offset:0
	global_load_dwordx4 a[212:215], v192, s[44:45] offset:1024
	global_load_dwordx4 a[216:219], v192, s[44:45] offset:2048
	global_load_dwordx4 a[220:223], v192, s[44:45] offset:3072
	s_add_u32 s44, s44, 0x1000
	s_addc_u32 s45, s45, 0
	global_load_dwordx4 a[224:227], v192, s[44:45] offset:0
	global_load_dwordx4 a[228:231], v192, s[44:45] offset:1024
	global_load_dwordx4 a[232:235], v192, s[44:45] offset:2048
	global_load_dwordx4 a[236:239], v192, s[44:45] offset:3072
	s_add_u32 s44, s44, 0x1000
	s_addc_u32 s45, s45, 0
	global_load_dwordx4 a[240:243], v192, s[44:45] offset:0
	global_load_dwordx4 a[244:247], v192, s[44:45] offset:1024
	global_load_dwordx4 a[248:251], v192, s[44:45] offset:2048
	global_load_dwordx4 a[252:255], v192, s[44:45] offset:3072
	s_add_u32 s44, s44, 0x1000
	s_addc_u32 s45, s45, 0
	s_lshl_b32 s64, s33, 3
	s_add_u32 s64, s64, s29
	s_lshl_b32 s64, s64, 5
	s_add_u32 s64, s64, s30
	s_lshl_b32 s64, s64, 2
	s_add_u32 s40, s8, s64
	s_addc_u32 s41, s9, 0
	s_and_b32 s64, s33, 1
	s_lshl_b32 s64, s64, 22
	s_add_u32 s64, s64, s50
	s_add_u32 s36, s6, s64
	s_addc_u32 s37, s7, 0
	v_exp_f32_e32 v200, v0
	v_exp_f32_e32 v201, v1
	v_exp_f32_e32 v202, v2
	v_exp_f32_e32 v203, v3
	v_exp_f32_e32 v204, v4
	v_exp_f32_e32 v205, v5
	v_exp_f32_e32 v206, v6
	v_exp_f32_e32 v207, v7
	v_exp_f32_e32 v208, v8
	v_exp_f32_e32 v209, v9
	v_exp_f32_e32 v210, v10
	v_exp_f32_e32 v211, v11
	v_exp_f32_e32 v212, v12
	v_exp_f32_e32 v213, v13
	v_exp_f32_e32 v214, v14
	v_exp_f32_e32 v215, v15
	v_add_f32_e32 v200, 1.0, v200
	v_add_f32_e32 v201, 1.0, v201
	v_add_f32_e32 v202, 1.0, v202
	v_add_f32_e32 v203, 1.0, v203
	v_add_f32_e32 v204, 1.0, v204
	v_add_f32_e32 v205, 1.0, v205
	v_add_f32_e32 v206, 1.0, v206
	v_add_f32_e32 v207, 1.0, v207
	v_add_f32_e32 v208, 1.0, v208
	v_add_f32_e32 v209, 1.0, v209
	v_add_f32_e32 v210, 1.0, v210
	v_add_f32_e32 v211, 1.0, v211
	v_add_f32_e32 v212, 1.0, v212
	v_add_f32_e32 v213, 1.0, v213
	v_add_f32_e32 v214, 1.0, v214
	v_add_f32_e32 v215, 1.0, v215
	v_rcp_f32_e32 v200, v200
	v_rcp_f32_e32 v201, v201
	v_rcp_f32_e32 v202, v202
	v_rcp_f32_e32 v203, v203
	v_rcp_f32_e32 v204, v204
	v_rcp_f32_e32 v205, v205
	v_rcp_f32_e32 v206, v206
	v_rcp_f32_e32 v207, v207
	v_rcp_f32_e32 v208, v208
	v_rcp_f32_e32 v209, v209
	v_rcp_f32_e32 v210, v210
	v_rcp_f32_e32 v211, v211
	v_rcp_f32_e32 v212, v212
	v_rcp_f32_e32 v213, v213
	v_rcp_f32_e32 v214, v214
	v_rcp_f32_e32 v215, v215
	v_fmamk_f32 v208, v208, 0xc0b8aa3b, v198
	v_fmamk_f32 v209, v209, 0xc0b8aa3b, v198
	v_fmamk_f32 v210, v210, 0xc0b8aa3b, v198
	v_fmamk_f32 v211, v211, 0xc0b8aa3b, v198
	v_mul_f32_e32 v204, v204, v128
	v_mul_f32_e32 v205, v205, v129
	v_mul_f32_e32 v206, v206, v130
	v_mul_f32_e32 v207, v207, v131
	v_fma_f32 v128, v200, v208, v204
	v_fma_f32 v129, v201, v209, v205
	v_fma_f32 v130, v202, v210, v206
	v_fma_f32 v131, v203, v211, v207
	v_exp_f32_e32 v200, v128
	v_exp_f32_e32 v201, v129
	v_exp_f32_e32 v202, v130
	v_exp_f32_e32 v203, v131
	v_add_f32_e32 v200, 1.0, v200
	v_add_f32_e32 v201, 1.0, v201
	v_add_f32_e32 v202, 1.0, v202
	v_add_f32_e32 v203, 1.0, v203
	v_rcp_f32_e32 v200, v200
	v_rcp_f32_e32 v201, v201
	v_rcp_f32_e32 v202, v202
	v_rcp_f32_e32 v203, v203
	v_fma_f32 v200, v200, 2.0, -1.0
	v_fma_f32 v201, v201, 2.0, -1.0
	v_fma_f32 v202, v202, 2.0, -1.0
	v_fma_f32 v203, v203, 2.0, -1.0
	v_mul_f32_e32 v216, v212, v200
	v_mul_f32_e32 v217, v213, v201
	v_mul_f32_e32 v218, v214, v202
	v_mul_f32_e32 v219, v215, v203
	v_cvt_pk_f16_f32 v220, v216, v217
	v_cvt_pk_f16_f32 v221, v218, v219
	v_exp_f32_e32 v200, v16
	v_exp_f32_e32 v201, v17
	v_exp_f32_e32 v202, v18
	v_exp_f32_e32 v203, v19
	v_exp_f32_e32 v204, v20
	v_exp_f32_e32 v205, v21
	v_exp_f32_e32 v206, v22
	v_exp_f32_e32 v207, v23
	v_exp_f32_e32 v208, v24
	v_exp_f32_e32 v209, v25
	v_exp_f32_e32 v210, v26
	v_exp_f32_e32 v211, v27
	v_exp_f32_e32 v212, v28
	v_exp_f32_e32 v213, v29
	v_exp_f32_e32 v214, v30
	v_exp_f32_e32 v215, v31
	v_add_f32_e32 v200, 1.0, v200
	v_add_f32_e32 v201, 1.0, v201
	v_add_f32_e32 v202, 1.0, v202
	v_add_f32_e32 v203, 1.0, v203
	v_add_f32_e32 v204, 1.0, v204
	v_add_f32_e32 v205, 1.0, v205
	v_add_f32_e32 v206, 1.0, v206
	v_add_f32_e32 v207, 1.0, v207
	v_add_f32_e32 v208, 1.0, v208
	v_add_f32_e32 v209, 1.0, v209
	v_add_f32_e32 v210, 1.0, v210
	v_add_f32_e32 v211, 1.0, v211
	v_add_f32_e32 v212, 1.0, v212
	v_add_f32_e32 v213, 1.0, v213
	v_add_f32_e32 v214, 1.0, v214
	v_add_f32_e32 v215, 1.0, v215
	v_rcp_f32_e32 v200, v200
	v_rcp_f32_e32 v201, v201
	v_rcp_f32_e32 v202, v202
	v_rcp_f32_e32 v203, v203
	v_rcp_f32_e32 v204, v204
	v_rcp_f32_e32 v205, v205
	v_rcp_f32_e32 v206, v206
	v_rcp_f32_e32 v207, v207
	v_rcp_f32_e32 v208, v208
	v_rcp_f32_e32 v209, v209
	v_rcp_f32_e32 v210, v210
	v_rcp_f32_e32 v211, v211
	v_rcp_f32_e32 v212, v212
	v_rcp_f32_e32 v213, v213
	v_rcp_f32_e32 v214, v214
	v_rcp_f32_e32 v215, v215
	v_fmamk_f32 v208, v208, 0xc0b8aa3b, v198
	v_fmamk_f32 v209, v209, 0xc0b8aa3b, v198
	v_fmamk_f32 v210, v210, 0xc0b8aa3b, v198
	v_fmamk_f32 v211, v211, 0xc0b8aa3b, v198
	v_mul_f32_e32 v204, v204, v132
	v_mul_f32_e32 v205, v205, v133
	v_mul_f32_e32 v206, v206, v134
	v_mul_f32_e32 v207, v207, v135
	v_fma_f32 v132, v200, v208, v204
	v_fma_f32 v133, v201, v209, v205
	v_fma_f32 v134, v202, v210, v206
	v_fma_f32 v135, v203, v211, v207
	v_exp_f32_e32 v200, v132
	v_exp_f32_e32 v201, v133
	v_exp_f32_e32 v202, v134
	v_exp_f32_e32 v203, v135
	v_add_f32_e32 v200, 1.0, v200
	v_add_f32_e32 v201, 1.0, v201
	v_add_f32_e32 v202, 1.0, v202
	v_add_f32_e32 v203, 1.0, v203
	v_rcp_f32_e32 v200, v200
	v_rcp_f32_e32 v201, v201
	v_rcp_f32_e32 v202, v202
	v_rcp_f32_e32 v203, v203
	v_fma_f32 v200, v200, 2.0, -1.0
	v_fma_f32 v201, v201, 2.0, -1.0
	v_fma_f32 v202, v202, 2.0, -1.0
	v_fma_f32 v203, v203, 2.0, -1.0
	v_mul_f32_e32 v216, v212, v200
	v_mul_f32_e32 v217, v213, v201
	v_mul_f32_e32 v218, v214, v202
	v_mul_f32_e32 v219, v215, v203
	v_cvt_pk_f16_f32 v222, v216, v217
	v_cvt_pk_f16_f32 v223, v218, v219
	s_nop 1
	v_permlane32_swap_b32_e32 v220, v222
	v_permlane32_swap_b32_e32 v221, v223
	s_cmp_eq_u32 s31, 0
	s_cbranch_scc1 .LE_slow4
	global_store_dwordx4 v195, v[220:223], s[36:37] offset:0
.LE_join5:
	s_and_b32 s64, s33, 1
	s_lshl_b32 s64, s64, 22
	s_add_u32 s64, s64, s50
	s_add_u32 s64, s64, 0x20000
	s_add_u32 s36, s6, s64
	s_addc_u32 s37, s7, 0
	v_exp_f32_e32 v200, v32
	v_exp_f32_e32 v201, v33
	v_exp_f32_e32 v202, v34
	v_exp_f32_e32 v203, v35
	v_exp_f32_e32 v204, v36
	v_exp_f32_e32 v205, v37
	v_exp_f32_e32 v206, v38
	v_exp_f32_e32 v207, v39
	v_exp_f32_e32 v208, v40
	v_exp_f32_e32 v209, v41
	v_exp_f32_e32 v210, v42
	v_exp_f32_e32 v211, v43
	v_exp_f32_e32 v212, v44
	v_exp_f32_e32 v213, v45
	v_exp_f32_e32 v214, v46
	v_exp_f32_e32 v215, v47
	v_add_f32_e32 v200, 1.0, v200
	v_add_f32_e32 v201, 1.0, v201
	v_add_f32_e32 v202, 1.0, v202
	v_add_f32_e32 v203, 1.0, v203
	v_add_f32_e32 v204, 1.0, v204
	v_add_f32_e32 v205, 1.0, v205
	v_add_f32_e32 v206, 1.0, v206
	v_add_f32_e32 v207, 1.0, v207
	v_add_f32_e32 v208, 1.0, v208
	v_add_f32_e32 v209, 1.0, v209
	v_add_f32_e32 v210, 1.0, v210
	v_add_f32_e32 v211, 1.0, v211
	v_add_f32_e32 v212, 1.0, v212
	v_add_f32_e32 v213, 1.0, v213
	v_add_f32_e32 v214, 1.0, v214
	v_add_f32_e32 v215, 1.0, v215
	v_rcp_f32_e32 v200, v200
	v_rcp_f32_e32 v201, v201
	v_rcp_f32_e32 v202, v202
	v_rcp_f32_e32 v203, v203
	v_rcp_f32_e32 v204, v204
	v_rcp_f32_e32 v205, v205
	v_rcp_f32_e32 v206, v206
	v_rcp_f32_e32 v207, v207
	v_rcp_f32_e32 v208, v208
	v_rcp_f32_e32 v209, v209
	v_rcp_f32_e32 v210, v210
	v_rcp_f32_e32 v211, v211
	v_rcp_f32_e32 v212, v212
	v_rcp_f32_e32 v213, v213
	v_rcp_f32_e32 v214, v214
	v_rcp_f32_e32 v215, v215
	v_fmamk_f32 v208, v208, 0xc0b8aa3b, v198
	v_fmamk_f32 v209, v209, 0xc0b8aa3b, v198
	v_fmamk_f32 v210, v210, 0xc0b8aa3b, v198
	v_fmamk_f32 v211, v211, 0xc0b8aa3b, v198
	v_mul_f32_e32 v204, v204, v136
	v_mul_f32_e32 v205, v205, v137
	v_mul_f32_e32 v206, v206, v138
	v_mul_f32_e32 v207, v207, v139
	v_fma_f32 v136, v200, v208, v204
	v_fma_f32 v137, v201, v209, v205
	v_fma_f32 v138, v202, v210, v206
	v_fma_f32 v139, v203, v211, v207
	v_exp_f32_e32 v200, v136
	v_exp_f32_e32 v201, v137
	v_exp_f32_e32 v202, v138
	v_exp_f32_e32 v203, v139
	v_add_f32_e32 v200, 1.0, v200
	v_add_f32_e32 v201, 1.0, v201
	v_add_f32_e32 v202, 1.0, v202
	v_add_f32_e32 v203, 1.0, v203
	v_rcp_f32_e32 v200, v200
	v_rcp_f32_e32 v201, v201
	v_rcp_f32_e32 v202, v202
	v_rcp_f32_e32 v203, v203
	v_fma_f32 v200, v200, 2.0, -1.0
	v_fma_f32 v201, v201, 2.0, -1.0
	v_fma_f32 v202, v202, 2.0, -1.0
	v_fma_f32 v203, v203, 2.0, -1.0
	v_mul_f32_e32 v216, v212, v200
	v_mul_f32_e32 v217, v213, v201
	v_mul_f32_e32 v218, v214, v202
	v_mul_f32_e32 v219, v215, v203
	v_cvt_pk_f16_f32 v220, v216, v217
	v_cvt_pk_f16_f32 v221, v218, v219
	v_exp_f32_e32 v200, v48
	v_exp_f32_e32 v201, v49
	v_exp_f32_e32 v202, v50
	v_exp_f32_e32 v203, v51
	v_exp_f32_e32 v204, v52
	v_exp_f32_e32 v205, v53
	v_exp_f32_e32 v206, v54
	v_exp_f32_e32 v207, v55
	v_exp_f32_e32 v208, v56
	v_exp_f32_e32 v209, v57
	v_exp_f32_e32 v210, v58
	v_exp_f32_e32 v211, v59
	v_exp_f32_e32 v212, v60
	v_exp_f32_e32 v213, v61
	v_exp_f32_e32 v214, v62
	v_exp_f32_e32 v215, v63
	v_add_f32_e32 v200, 1.0, v200
	v_add_f32_e32 v201, 1.0, v201
	v_add_f32_e32 v202, 1.0, v202
	v_add_f32_e32 v203, 1.0, v203
	v_add_f32_e32 v204, 1.0, v204
	v_add_f32_e32 v205, 1.0, v205
	v_add_f32_e32 v206, 1.0, v206
	v_add_f32_e32 v207, 1.0, v207
	v_add_f32_e32 v208, 1.0, v208
	v_add_f32_e32 v209, 1.0, v209
	v_add_f32_e32 v210, 1.0, v210
	v_add_f32_e32 v211, 1.0, v211
	v_add_f32_e32 v212, 1.0, v212
	v_add_f32_e32 v213, 1.0, v213
	v_add_f32_e32 v214, 1.0, v214
	v_add_f32_e32 v215, 1.0, v215
	v_rcp_f32_e32 v200, v200
	v_rcp_f32_e32 v201, v201
	v_rcp_f32_e32 v202, v202
	v_rcp_f32_e32 v203, v203
	v_rcp_f32_e32 v204, v204
	v_rcp_f32_e32 v205, v205
	v_rcp_f32_e32 v206, v206
	v_rcp_f32_e32 v207, v207
	v_rcp_f32_e32 v208, v208
	v_rcp_f32_e32 v209, v209
	v_rcp_f32_e32 v210, v210
	v_rcp_f32_e32 v211, v211
	v_rcp_f32_e32 v212, v212
	v_rcp_f32_e32 v213, v213
	v_rcp_f32_e32 v214, v214
	v_rcp_f32_e32 v215, v215
	v_fmamk_f32 v208, v208, 0xc0b8aa3b, v198
	v_fmamk_f32 v209, v209, 0xc0b8aa3b, v198
	v_fmamk_f32 v210, v210, 0xc0b8aa3b, v198
	v_fmamk_f32 v211, v211, 0xc0b8aa3b, v198
	v_mul_f32_e32 v204, v204, v140
	v_mul_f32_e32 v205, v205, v141
	v_mul_f32_e32 v206, v206, v142
	v_mul_f32_e32 v207, v207, v143
	v_fma_f32 v140, v200, v208, v204
	v_fma_f32 v141, v201, v209, v205
	v_fma_f32 v142, v202, v210, v206
	v_fma_f32 v143, v203, v211, v207
	v_exp_f32_e32 v200, v140
	v_exp_f32_e32 v201, v141
	v_exp_f32_e32 v202, v142
	v_exp_f32_e32 v203, v143
	v_add_f32_e32 v200, 1.0, v200
	v_add_f32_e32 v201, 1.0, v201
	v_add_f32_e32 v202, 1.0, v202
	v_add_f32_e32 v203, 1.0, v203
	v_rcp_f32_e32 v200, v200
	v_rcp_f32_e32 v201, v201
	v_rcp_f32_e32 v202, v202
	v_rcp_f32_e32 v203, v203
	v_fma_f32 v200, v200, 2.0, -1.0
	v_fma_f32 v201, v201, 2.0, -1.0
	v_fma_f32 v202, v202, 2.0, -1.0
	v_fma_f32 v203, v203, 2.0, -1.0
	v_mul_f32_e32 v216, v212, v200
	v_mul_f32_e32 v217, v213, v201
	v_mul_f32_e32 v218, v214, v202
	v_mul_f32_e32 v219, v215, v203
	v_cvt_pk_f16_f32 v222, v216, v217
	v_cvt_pk_f16_f32 v223, v218, v219
	s_nop 1
	v_permlane32_swap_b32_e32 v220, v222
	v_permlane32_swap_b32_e32 v221, v223
	s_cmp_eq_u32 s31, 0
	s_cbranch_scc1 .LE_slow6
	global_store_dwordx4 v195, v[220:223], s[36:37] offset:0
.LE_join7:
	s_and_b32 s64, s33, 1
	s_lshl_b32 s64, s64, 22
	s_add_u32 s64, s64, s50
	s_add_u32 s64, s64, 0x40000
	s_add_u32 s36, s6, s64
	s_addc_u32 s37, s7, 0
	v_exp_f32_e32 v200, v64
	v_exp_f32_e32 v201, v65
	v_exp_f32_e32 v202, v66
	v_exp_f32_e32 v203, v67
	v_exp_f32_e32 v204, v68
	v_exp_f32_e32 v205, v69
	v_exp_f32_e32 v206, v70
	v_exp_f32_e32 v207, v71
	v_exp_f32_e32 v208, v72
	v_exp_f32_e32 v209, v73
	v_exp_f32_e32 v210, v74
	v_exp_f32_e32 v211, v75
	v_exp_f32_e32 v212, v76
	v_exp_f32_e32 v213, v77
	v_exp_f32_e32 v214, v78
	v_exp_f32_e32 v215, v79
	v_add_f32_e32 v200, 1.0, v200
	v_add_f32_e32 v201, 1.0, v201
	v_add_f32_e32 v202, 1.0, v202
	v_add_f32_e32 v203, 1.0, v203
	v_add_f32_e32 v204, 1.0, v204
	v_add_f32_e32 v205, 1.0, v205
	v_add_f32_e32 v206, 1.0, v206
	v_add_f32_e32 v207, 1.0, v207
	v_add_f32_e32 v208, 1.0, v208
	v_add_f32_e32 v209, 1.0, v209
	v_add_f32_e32 v210, 1.0, v210
	v_add_f32_e32 v211, 1.0, v211
	v_add_f32_e32 v212, 1.0, v212
	v_add_f32_e32 v213, 1.0, v213
	v_add_f32_e32 v214, 1.0, v214
	v_add_f32_e32 v215, 1.0, v215
	v_rcp_f32_e32 v200, v200
	v_rcp_f32_e32 v201, v201
	v_rcp_f32_e32 v202, v202
	v_rcp_f32_e32 v203, v203
	v_rcp_f32_e32 v204, v204
	v_rcp_f32_e32 v205, v205
	v_rcp_f32_e32 v206, v206
	v_rcp_f32_e32 v207, v207
	v_rcp_f32_e32 v208, v208
	v_rcp_f32_e32 v209, v209
	v_rcp_f32_e32 v210, v210
	v_rcp_f32_e32 v211, v211
	v_rcp_f32_e32 v212, v212
	v_rcp_f32_e32 v213, v213
	v_rcp_f32_e32 v214, v214
	v_rcp_f32_e32 v215, v215
	v_fmamk_f32 v208, v208, 0xc0b8aa3b, v198
	v_fmamk_f32 v209, v209, 0xc0b8aa3b, v198
	v_fmamk_f32 v210, v210, 0xc0b8aa3b, v198
	v_fmamk_f32 v211, v211, 0xc0b8aa3b, v198
	v_mul_f32_e32 v204, v204, v144
	v_mul_f32_e32 v205, v205, v145
	v_mul_f32_e32 v206, v206, v146
	v_mul_f32_e32 v207, v207, v147
	v_fma_f32 v144, v200, v208, v204
	v_fma_f32 v145, v201, v209, v205
	v_fma_f32 v146, v202, v210, v206
	v_fma_f32 v147, v203, v211, v207
	v_exp_f32_e32 v200, v144
	v_exp_f32_e32 v201, v145
	v_exp_f32_e32 v202, v146
	v_exp_f32_e32 v203, v147
	v_add_f32_e32 v200, 1.0, v200
	v_add_f32_e32 v201, 1.0, v201
	v_add_f32_e32 v202, 1.0, v202
	v_add_f32_e32 v203, 1.0, v203
	v_rcp_f32_e32 v200, v200
	v_rcp_f32_e32 v201, v201
	v_rcp_f32_e32 v202, v202
	v_rcp_f32_e32 v203, v203
	v_fma_f32 v200, v200, 2.0, -1.0
	v_fma_f32 v201, v201, 2.0, -1.0
	v_fma_f32 v202, v202, 2.0, -1.0
	v_fma_f32 v203, v203, 2.0, -1.0
	v_mul_f32_e32 v216, v212, v200
	v_mul_f32_e32 v217, v213, v201
	v_mul_f32_e32 v218, v214, v202
	v_mul_f32_e32 v219, v215, v203
	v_cvt_pk_f16_f32 v220, v216, v217
	v_cvt_pk_f16_f32 v221, v218, v219
	v_exp_f32_e32 v200, v80
	v_exp_f32_e32 v201, v81
	v_exp_f32_e32 v202, v82
	v_exp_f32_e32 v203, v83
	v_exp_f32_e32 v204, v84
	v_exp_f32_e32 v205, v85
	v_exp_f32_e32 v206, v86
	v_exp_f32_e32 v207, v87
	v_exp_f32_e32 v208, v88
	v_exp_f32_e32 v209, v89
	v_exp_f32_e32 v210, v90
	v_exp_f32_e32 v211, v91
	v_exp_f32_e32 v212, v92
	v_exp_f32_e32 v213, v93
	v_exp_f32_e32 v214, v94
	v_exp_f32_e32 v215, v95
	v_add_f32_e32 v200, 1.0, v200
	v_add_f32_e32 v201, 1.0, v201
	v_add_f32_e32 v202, 1.0, v202
	v_add_f32_e32 v203, 1.0, v203
	v_add_f32_e32 v204, 1.0, v204
	v_add_f32_e32 v205, 1.0, v205
	v_add_f32_e32 v206, 1.0, v206
	v_add_f32_e32 v207, 1.0, v207
	v_add_f32_e32 v208, 1.0, v208
	v_add_f32_e32 v209, 1.0, v209
	v_add_f32_e32 v210, 1.0, v210
	v_add_f32_e32 v211, 1.0, v211
	v_add_f32_e32 v212, 1.0, v212
	v_add_f32_e32 v213, 1.0, v213
	v_add_f32_e32 v214, 1.0, v214
	v_add_f32_e32 v215, 1.0, v215
	v_rcp_f32_e32 v200, v200
	v_rcp_f32_e32 v201, v201
	v_rcp_f32_e32 v202, v202
	v_rcp_f32_e32 v203, v203
	v_rcp_f32_e32 v204, v204
	v_rcp_f32_e32 v205, v205
	v_rcp_f32_e32 v206, v206
	v_rcp_f32_e32 v207, v207
	v_rcp_f32_e32 v208, v208
	v_rcp_f32_e32 v209, v209
	v_rcp_f32_e32 v210, v210
	v_rcp_f32_e32 v211, v211
	v_rcp_f32_e32 v212, v212
	v_rcp_f32_e32 v213, v213
	v_rcp_f32_e32 v214, v214
	v_rcp_f32_e32 v215, v215
	v_fmamk_f32 v208, v208, 0xc0b8aa3b, v198
	v_fmamk_f32 v209, v209, 0xc0b8aa3b, v198
	v_fmamk_f32 v210, v210, 0xc0b8aa3b, v198
	v_fmamk_f32 v211, v211, 0xc0b8aa3b, v198
	v_mul_f32_e32 v204, v204, v148
	v_mul_f32_e32 v205, v205, v149
	v_mul_f32_e32 v206, v206, v150
	v_mul_f32_e32 v207, v207, v151
	v_fma_f32 v148, v200, v208, v204
	v_fma_f32 v149, v201, v209, v205
	v_fma_f32 v150, v202, v210, v206
	v_fma_f32 v151, v203, v211, v207
	v_exp_f32_e32 v200, v148
	v_exp_f32_e32 v201, v149
	v_exp_f32_e32 v202, v150
	v_exp_f32_e32 v203, v151
	v_add_f32_e32 v200, 1.0, v200
	v_add_f32_e32 v201, 1.0, v201
	v_add_f32_e32 v202, 1.0, v202
	v_add_f32_e32 v203, 1.0, v203
	v_rcp_f32_e32 v200, v200
	v_rcp_f32_e32 v201, v201
	v_rcp_f32_e32 v202, v202
	v_rcp_f32_e32 v203, v203
	v_fma_f32 v200, v200, 2.0, -1.0
	v_fma_f32 v201, v201, 2.0, -1.0
	v_fma_f32 v202, v202, 2.0, -1.0
	v_fma_f32 v203, v203, 2.0, -1.0
	v_mul_f32_e32 v216, v212, v200
	v_mul_f32_e32 v217, v213, v201
	v_mul_f32_e32 v218, v214, v202
	v_mul_f32_e32 v219, v215, v203
	v_cvt_pk_f16_f32 v222, v216, v217
	v_cvt_pk_f16_f32 v223, v218, v219
	s_nop 1
	v_permlane32_swap_b32_e32 v220, v222
	v_permlane32_swap_b32_e32 v221, v223
	s_cmp_eq_u32 s31, 0
	s_cbranch_scc1 .LE_slow8
	global_store_dwordx4 v195, v[220:223], s[36:37] offset:0
.LE_join9:
	s_waitcnt vmcnt(2)
	s_waitcnt vmcnt(1)
	s_waitcnt vmcnt(0)
	s_barrier
	v_mov_b32_e32 v199, 3
	s_cmp_eq_u32 s31, 0
	s_cbranch_scc1 .LE_slow10
	global_store_dword v197, v199, s[40:41]

.LE_slow4:
	global_store_dwordx4 v195, v[220:223], s[36:37] offset:0 sc1
	s_branch .LE_join5
.LE_slow6:
	global_store_dwordx4 v195, v[220:223], s[36:37] offset:0 sc1
	s_branch .LE_join7
.LE_slow8:
	global_store_dwordx4 v195, v[220:223], s[36:37] offset:0 sc1
	s_branch .LE_join9

.LD_cdone1:
	s_waitcnt lgkmcnt(0)
	s_barrier
	v_mov_b32_e32 v252, 0x22000
	ds_read_b32 v200, v252
	ds_read_b32 v201, v252 offset:4
	ds_read_b32 v202, v252 offset:8
	s_waitcnt lgkmcnt(0)
	s_nop 1
	v_readfirstlane_b32 s31, v200
	v_readfirstlane_b32 s29, v201
	v_readfirstlane_b32 s30, v202
	s_nop 3
	s_barrier
	s_lshl_b32 s49, s29, 19
	s_lshl_b32 s64, s32, 13
	s_add_u32 s49, s49, s64
	s_mov_b32 s51, s64
	s_add_u32 s52, s51, 0x0
	s_add_u32 s53, s51, 0x1000
	s_add_u32 s54, s51, 0x8000
	s_add_u32 s55, s51, 0x9000
	s_add_u32 s56, s51, 0x10000
	s_add_u32 s57, s51, 0x11000
	s_add_u32 s58, s51, 0x18000
	s_add_u32 s59, s51, 0x19000
	s_lshl_b32 s64, s29, 8
	s_lshl_b32 s65, s30, 1
	s_add_u32 s64, s64, s65
	s_lshr_b32 s65, s32, 1
	s_add_u32 s64, s64, s65
	s_lshl_b32 s64, s64, 11
	s_and_b32 s65, s32, 1
	s_lshl_b32 s65, s65, 9
	s_add_u32 s50, s64, s65
	s_sub_u32 s60, s28, 1
	v_mov_b32_e32 v128, 0
	v_mov_b32_e32 v129, 0
	v_mov_b32_e32 v130, 0
	v_mov_b32_e32 v131, 0
	v_mov_b32_e32 v132, 0
	v_mov_b32_e32 v133, 0
	v_mov_b32_e32 v134, 0
	v_mov_b32_e32 v135, 0
	v_mov_b32_e32 v136, 0
	v_mov_b32_e32 v137, 0
	v_mov_b32_e32 v138, 0
	v_mov_b32_e32 v139, 0
	v_mov_b32_e32 v140, 0
	v_mov_b32_e32 v141, 0
	v_mov_b32_e32 v142, 0
	v_mov_b32_e32 v143, 0
	v_mov_b32_e32 v144, 0
	v_mov_b32_e32 v145, 0
	v_mov_b32_e32 v146, 0
	v_mov_b32_e32 v147, 0
	v_mov_b32_e32 v148, 0
	v_mov_b32_e32 v149, 0
	v_mov_b32_e32 v150, 0
	v_mov_b32_e32 v151, 0
	v_mov_b32_e32 v152, 0
	v_mov_b32_e32 v153, 0
	v_mov_b32_e32 v154, 0
	v_mov_b32_e32 v155, 0
	v_mov_b32_e32 v156, 0
	v_mov_b32_e32 v157, 0
	v_mov_b32_e32 v158, 0
	v_mov_b32_e32 v159, 0
	s_lshl_b32 s64, s30, 5
	s_lshl_b32 s65, s32, 3
	s_add_u32 s64, s64, s65
	v_lshlrev_b32_e32 v255, 2, v254
	v_add_u32_e32 v255, s64, v255
	v_lshlrev_b32_e32 v200, 2, v255
	global_load_dwordx4 v[228:231], v200, s[22:23]
	v_add_u32_e32 v201, 0x1000, v200
	global_load_dwordx4 v[232:235], v201, s[22:23]
	s_lshl_b32 s65, s32, 11
	v_lshl_add_u32 v248, v253, 3, s65
	v_add_u32_e32 v248, 0x20000, v248
	v_and_b32_e32 v250, 15, v194
	s_mul_i32 s65, s32, 128
	v_lshl_add_u32 v249, v250, 3, s65
	v_add_u32_e32 v249, 0x20000, v249
	v_lshlrev_b32_e32 v250, 3, v250
	s_lshl_b32 s65, s30, 11
	s_lshl_b32 s66, s29, 8
	s_add_u32 s65, s65, s66
	s_mul_i32 s66, s32, 16
	s_add_u32 s65, s65, s66
	s_lshl_b32 s65, s65, 3
	s_add_u32 s62, s24, s65
	s_addc_u32 s63, s25, 0
	s_lshl_b32 s65, s29, 5
	s_add_u32 s65, s65, s30
	s_lshl_b32 s65, s65, 2
	s_add_u32 s65, s65, s32
	s_lshl_b32 s65, s65, 15
	s_add_u32 s42, s18, s65
	s_addc_u32 s43, s19, 0
	s_waitcnt vmcnt(0)
	s_waitcnt vmcnt(0)
	s_mov_b32 s33, 0
	s_add_u32 s46, s42, 0x0
	s_addc_u32 s47, s43, 0
	global_load_dwordx4 v[0:3], v192, s[46:47] offset:0
	global_load_dwordx4 v[4:7], v192, s[46:47] offset:1024
	global_load_dwordx4 v[8:11], v192, s[46:47] offset:2048
	global_load_dwordx4 v[12:15], v192, s[46:47] offset:3072
	s_add_u32 s46, s42, 0x1000
	s_addc_u32 s47, s43, 0
	global_load_dwordx4 v[16:19], v192, s[46:47] offset:0
	global_load_dwordx4 v[20:23], v192, s[46:47] offset:1024
	global_load_dwordx4 v[24:27], v192, s[46:47] offset:2048
	global_load_dwordx4 v[28:31], v192, s[46:47] offset:3072
	s_add_u32 s46, s42, 0x2000
	s_addc_u32 s47, s43, 0
	global_load_dwordx4 v[32:35], v192, s[46:47] offset:0
	global_load_dwordx4 v[36:39], v192, s[46:47] offset:1024
	global_load_dwordx4 v[40:43], v192, s[46:47] offset:2048
	global_load_dwordx4 v[44:47], v192, s[46:47] offset:3072
	s_add_u32 s46, s42, 0x3000
	s_addc_u32 s47, s43, 0
	global_load_dwordx4 v[48:51], v192, s[46:47] offset:0
	global_load_dwordx4 v[52:55], v192, s[46:47] offset:1024
	global_load_dwordx4 v[56:59], v192, s[46:47] offset:2048
	global_load_dwordx4 v[60:63], v192, s[46:47] offset:3072
	s_add_u32 s46, s42, 0x4000
	s_addc_u32 s47, s43, 0
	global_load_dwordx4 v[64:67], v192, s[46:47] offset:0
	global_load_dwordx4 v[68:71], v192, s[46:47] offset:1024
	global_load_dwordx4 v[72:75], v192, s[46:47] offset:2048
	global_load_dwordx4 v[76:79], v192, s[46:47] offset:3072
	s_add_u32 s46, s42, 0x5000
	s_addc_u32 s47, s43, 0
	global_load_dwordx4 v[80:83], v192, s[46:47] offset:0
	global_load_dwordx4 v[84:87], v192, s[46:47] offset:1024
	global_load_dwordx4 v[88:91], v192, s[46:47] offset:2048
	global_load_dwordx4 v[92:95], v192, s[46:47] offset:3072
	s_add_u32 s46, s42, 0x6000
	s_addc_u32 s47, s43, 0
	global_load_dwordx4 v[96:99], v192, s[46:47] offset:0
	global_load_dwordx4 v[100:103], v192, s[46:47] offset:1024
	global_load_dwordx4 v[104:107], v192, s[46:47] offset:2048
	global_load_dwordx4 v[108:111], v192, s[46:47] offset:3072
	s_add_u32 s46, s42, 0x7000
	s_addc_u32 s47, s43, 0
	global_load_dwordx4 v[112:115], v192, s[46:47] offset:0
	global_load_dwordx4 v[116:119], v192, s[46:47] offset:1024
	global_load_dwordx4 v[120:123], v192, s[46:47] offset:2048
	global_load_dwordx4 v[124:127], v192, s[46:47] offset:3072
	s_waitcnt vmcnt(0)
	s_waitcnt lgkmcnt(0)
	s_lshl_b32 s64, s30, 2
	s_add_u32 s64, s64, s32
	s_lshl_b32 s64, s64, 16
	s_add_u32 s44, s4, s64
	s_addc_u32 s45, s5, 0
	global_load_dwordx4 a[0:3], v192, s[44:45] offset:0
	global_load_dwordx4 a[4:7], v192, s[44:45] offset:1024
	global_load_dwordx4 a[8:11], v192, s[44:45] offset:2048
	global_load_dwordx4 a[12:15], v192, s[44:45] offset:3072
	s_add_u32 s44, s44, 0x1000
	s_addc_u32 s45, s45, 0
	global_load_dwordx4 a[16:19], v192, s[44:45] offset:0
	global_load_dwordx4 a[20:23], v192, s[44:45] offset:1024
	global_load_dwordx4 a[24:27], v192, s[44:45] offset:2048
	global_load_dwordx4 a[28:31], v192, s[44:45] offset:3072
	s_add_u32 s44, s44, 0x1000
	s_addc_u32 s45, s45, 0
	global_load_dwordx4 a[32:35], v192, s[44:45] offset:0
	global_load_dwordx4 a[36:39], v192, s[44:45] offset:1024
	global_load_dwordx4 a[40:43], v192, s[44:45] offset:2048
	global_load_dwordx4 a[44:47], v192, s[44:45] offset:3072
	s_add_u32 s44, s44, 0x1000
	s_addc_u32 s45, s45, 0
	global_load_dwordx4 a[48:51], v192, s[44:45] offset:0
	global_load_dwordx4 a[52:55], v192, s[44:45] offset:1024
	global_load_dwordx4 a[56:59], v192, s[44:45] offset:2048
	global_load_dwordx4 a[60:63], v192, s[44:45] offset:3072
	s_add_u32 s44, s44, 0x1000
	s_addc_u32 s45, s45, 0
	global_load_dwordx4 a[64:67], v192, s[44:45] offset:0
	global_load_dwordx4 a[68:71], v192, s[44:45] offset:1024
	global_load_dwordx4 a[72:75], v192, s[44:45] offset:2048
	global_load_dwordx4 a[76:79], v192, s[44:45] offset:3072
	s_add_u32 s44, s44, 0x1000
	s_addc_u32 s45, s45, 0
	global_load_dwordx4 a[80:83], v192, s[44:45] offset:0
	global_load_dwordx4 a[84:87], v192, s[44:45] offset:1024
	global_load_dwordx4 a[88:91], v192, s[44:45] offset:2048
	global_load_dwordx4 a[92:95], v192, s[44:45] offset:3072
	s_add_u32 s44, s44, 0x1000
	s_addc_u32 s45, s45, 0
	global_load_dwordx4 a[96:99], v192, s[44:45] offset:0
	global_load_dwordx4 a[100:103], v192, s[44:45] offset:1024
	global_load_dwordx4 a[104:107], v192, s[44:45] offset:2048
	global_load_dwordx4 a[108:111], v192, s[44:45] offset:3072
	s_add_u32 s44, s44, 0x1000
	s_addc_u32 s45, s45, 0
	global_load_dwordx4 a[112:115], v192, s[44:45] offset:0
	global_load_dwordx4 a[116:119], v192, s[44:45] offset:1024
	global_load_dwordx4 a[120:123], v192, s[44:45] offset:2048
	global_load_dwordx4 a[124:127], v192, s[44:45] offset:3072
	s_add_u32 s44, s44, 0x1000
	s_addc_u32 s45, s45, 0
	s_waitcnt vmcnt(16)
	global_load_dwordx4 a[128:131], v192, s[44:45] offset:0
	global_load_dwordx4 a[132:135], v192, s[44:45] offset:1024
	global_load_dwordx4 a[136:139], v192, s[44:45] offset:2048
	global_load_dwordx4 a[140:143], v192, s[44:45] offset:3072
	s_add_u32 s44, s44, 0x1000
	s_addc_u32 s45, s45, 0
	global_load_dwordx4 a[144:147], v192, s[44:45] offset:0
	global_load_dwordx4 a[148:151], v192, s[44:45] offset:1024
	global_load_dwordx4 a[152:155], v192, s[44:45] offset:2048
	global_load_dwordx4 a[156:159], v192, s[44:45] offset:3072
	s_add_u32 s44, s44, 0x1000
	s_addc_u32 s45, s45, 0
	global_load_dwordx4 a[160:163], v192, s[44:45] offset:0
	global_load_dwordx4 a[164:167], v192, s[44:45] offset:1024
	global_load_dwordx4 a[168:171], v192, s[44:45] offset:2048
	global_load_dwordx4 a[172:175], v192, s[44:45] offset:3072
	s_add_u32 s44, s44, 0x1000
	s_addc_u32 s45, s45, 0
	global_load_dwordx4 a[176:179], v192, s[44:45] offset:0
	global_load_dwordx4 a[180:183], v192, s[44:45] offset:1024
	global_load_dwordx4 a[184:187], v192, s[44:45] offset:2048
	global_load_dwordx4 a[188:191], v192, s[44:45] offset:3072
	s_add_u32 s44, s44, 0x1000
	s_addc_u32 s45, s45, 0
	global_load_dwordx4 a[192:195], v192, s[44:45] offset:0
	global_load_dwordx4 a[196:199], v192, s[44:45] offset:1024
	global_load_dwordx4 a[200:203], v192, s[44:45] offset:2048
	global_load_dwordx4 a[204:207], v192, s[44:45] offset:3072
	s_add_u32 s44, s44, 0x1000
	s_addc_u32 s45, s45, 0
	global_load_dwordx4 a[208:211], v192, s[44:45] offset:0
	global_load_dwordx4 a[212:215], v192, s[44:45] offset:1024
	global_load_dwordx4 a[216:219], v192, s[44:45] offset:2048
	global_load_dwordx4 a[220:223], v192, s[44:45] offset:3072
	s_add_u32 s44, s44, 0x1000
	s_addc_u32 s45, s45, 0
	global_load_dwordx4 a[224:227], v192, s[44:45] offset:0
	global_load_dwordx4 a[228:231], v192, s[44:45] offset:1024
	global_load_dwordx4 a[232:235], v192, s[44:45] offset:2048
	global_load_dwordx4 a[236:239], v192, s[44:45] offset:3072
	s_add_u32 s44, s44, 0x1000
	s_addc_u32 s45, s45, 0
	global_load_dwordx4 a[240:243], v192, s[44:45] offset:0
	global_load_dwordx4 a[244:247], v192, s[44:45] offset:1024
	global_load_dwordx4 a[248:251], v192, s[44:45] offset:2048
	global_load_dwordx4 a[252:255], v192, s[44:45] offset:3072
	s_add_u32 s44, s44, 0x1000
	s_addc_u32 s45, s45, 0
	s_lshl_b32 s64, s33, 3
	s_add_u32 s64, s64, s29
	s_lshl_b32 s64, s64, 5
	s_add_u32 s64, s64, s30
	s_lshl_b32 s64, s64, 2
	s_add_u32 s40, s8, s64
	s_addc_u32 s41, s9, 0
	s_and_b32 s64, s33, 1
	s_lshl_b32 s64, s64, 22
	s_add_u32 s64, s64, s50
	s_add_u32 s36, s6, s64
	s_addc_u32 s37, s7, 0
	s_lshl_b32 s64, s33, 19
	s_add_u32 s72, s62, s64
	s_addc_u32 s73, s63, 0
	v_exp_f32_e32 v200, v0
	v_exp_f32_e32 v201, v1
	v_exp_f32_e32 v202, v2
	v_exp_f32_e32 v203, v3
	v_exp_f32_e32 v204, v4
	v_exp_f32_e32 v205, v5
	v_exp_f32_e32 v206, v6
	v_exp_f32_e32 v207, v7
	v_exp_f32_e32 v208, v8
	v_exp_f32_e32 v209, v9
	v_exp_f32_e32 v210, v10
	v_exp_f32_e32 v211, v11
	v_exp_f32_e32 v212, v12
	v_exp_f32_e32 v213, v13
	v_exp_f32_e32 v214, v14
	v_exp_f32_e32 v215, v15
	v_add_f32_e32 v200, 1.0, v200
	v_add_f32_e32 v201, 1.0, v201
	v_add_f32_e32 v202, 1.0, v202
	v_add_f32_e32 v203, 1.0, v203
	v_add_f32_e32 v204, 1.0, v204
	v_add_f32_e32 v205, 1.0, v205
	v_add_f32_e32 v206, 1.0, v206
	v_add_f32_e32 v207, 1.0, v207
	v_add_f32_e32 v208, 1.0, v208
	v_add_f32_e32 v209, 1.0, v209
	v_add_f32_e32 v210, 1.0, v210
	v_add_f32_e32 v211, 1.0, v211
	v_add_f32_e32 v212, 1.0, v212
	v_add_f32_e32 v213, 1.0, v213
	v_add_f32_e32 v214, 1.0, v214
	v_add_f32_e32 v215, 1.0, v215
	v_rcp_f32_e32 v200, v200
	v_rcp_f32_e32 v201, v201
	v_rcp_f32_e32 v202, v202
	v_rcp_f32_e32 v203, v203
	v_rcp_f32_e32 v204, v204
	v_rcp_f32_e32 v205, v205
	v_rcp_f32_e32 v206, v206
	v_rcp_f32_e32 v207, v207
	v_rcp_f32_e32 v208, v208
	v_rcp_f32_e32 v209, v209
	v_rcp_f32_e32 v210, v210
	v_rcp_f32_e32 v211, v211
	v_rcp_f32_e32 v212, v212
	v_rcp_f32_e32 v213, v213
	v_rcp_f32_e32 v214, v214
	v_rcp_f32_e32 v215, v215
	v_fmamk_f32 v208, v208, 0xc0b8aa3b, v198
	v_fmamk_f32 v209, v209, 0xc0b8aa3b, v198
	v_fmamk_f32 v210, v210, 0xc0b8aa3b, v198
	v_fmamk_f32 v211, v211, 0xc0b8aa3b, v198
	v_mul_f32_e32 v204, v204, v128
	v_mul_f32_e32 v205, v205, v129
	v_mul_f32_e32 v206, v206, v130
	v_mul_f32_e32 v207, v207, v131
	v_fma_f32 v128, v200, v208, v204
	v_fma_f32 v129, v201, v209, v205
	v_fma_f32 v130, v202, v210, v206
	v_fma_f32 v131, v203, v211, v207
	v_exp_f32_e32 v200, v128
	v_exp_f32_e32 v201, v129
	v_exp_f32_e32 v202, v130
	v_exp_f32_e32 v203, v131
	v_add_f32_e32 v200, 1.0, v200
	v_add_f32_e32 v201, 1.0, v201
	v_add_f32_e32 v202, 1.0, v202
	v_add_f32_e32 v203, 1.0, v203
	v_rcp_f32_e32 v200, v200
	v_rcp_f32_e32 v201, v201
	v_rcp_f32_e32 v202, v202
	v_rcp_f32_e32 v203, v203
	v_fma_f32 v200, v200, 2.0, -1.0
	v_fma_f32 v201, v201, 2.0, -1.0
	v_fma_f32 v202, v202, 2.0, -1.0
	v_fma_f32 v203, v203, 2.0, -1.0
	v_mul_f32_e32 v216, v212, v200
	v_mul_f32_e32 v217, v213, v201
	v_mul_f32_e32 v218, v214, v202
	v_mul_f32_e32 v219, v215, v203
	v_mul_f32_e32 v236, v216, v228
	v_mul_f32_e32 v237, v216, v232
	v_fmac_f32_e32 v236, v217, v229
	v_fmac_f32_e32 v237, v217, v233
	v_fmac_f32_e32 v236, v218, v230
	v_fmac_f32_e32 v237, v218, v234
	v_fmac_f32_e32 v236, v219, v231
	v_fmac_f32_e32 v237, v219, v235
	v_mov_b32_e32 v238, v236
	v_mov_b32_e32 v239, v236
	v_mov_b32_e32 v240, v237
	v_mov_b32_e32 v241, v237
	s_nop 1
	v_permlane32_swap_b32_e32 v238, v239
	v_permlane32_swap_b32_e32 v240, v241
	v_add_f32_e32 v238, v238, v239
	v_add_f32_e32 v239, v240, v241
	ds_write_b64 v248, v[238:239] offset:0
	v_cvt_pk_f16_f32 v220, v216, v217
	v_cvt_pk_f16_f32 v221, v218, v219
	v_exp_f32_e32 v200, v16
	v_exp_f32_e32 v201, v17
	v_exp_f32_e32 v202, v18
	v_exp_f32_e32 v203, v19
	v_exp_f32_e32 v204, v20
	v_exp_f32_e32 v205, v21
	v_exp_f32_e32 v206, v22
	v_exp_f32_e32 v207, v23
	v_exp_f32_e32 v208, v24
	v_exp_f32_e32 v209, v25
	v_exp_f32_e32 v210, v26
	v_exp_f32_e32 v211, v27
	v_exp_f32_e32 v212, v28
	v_exp_f32_e32 v213, v29
	v_exp_f32_e32 v214, v30
	v_exp_f32_e32 v215, v31
	v_add_f32_e32 v200, 1.0, v200
	v_add_f32_e32 v201, 1.0, v201
	v_add_f32_e32 v202, 1.0, v202
	v_add_f32_e32 v203, 1.0, v203
	v_add_f32_e32 v204, 1.0, v204
	v_add_f32_e32 v205, 1.0, v205
	v_add_f32_e32 v206, 1.0, v206
	v_add_f32_e32 v207, 1.0, v207
	v_add_f32_e32 v208, 1.0, v208
	v_add_f32_e32 v209, 1.0, v209
	v_add_f32_e32 v210, 1.0, v210
	v_add_f32_e32 v211, 1.0, v211
	v_add_f32_e32 v212, 1.0, v212
	v_add_f32_e32 v213, 1.0, v213
	v_add_f32_e32 v214, 1.0, v214
	v_add_f32_e32 v215, 1.0, v215
	v_rcp_f32_e32 v200, v200
	v_rcp_f32_e32 v201, v201
	v_rcp_f32_e32 v202, v202
	v_rcp_f32_e32 v203, v203
	v_rcp_f32_e32 v204, v204
	v_rcp_f32_e32 v205, v205
	v_rcp_f32_e32 v206, v206
	v_rcp_f32_e32 v207, v207
	v_rcp_f32_e32 v208, v208
	v_rcp_f32_e32 v209, v209
	v_rcp_f32_e32 v210, v210
	v_rcp_f32_e32 v211, v211
	v_rcp_f32_e32 v212, v212
	v_rcp_f32_e32 v213, v213
	v_rcp_f32_e32 v214, v214
	v_rcp_f32_e32 v215, v215
	v_fmamk_f32 v208, v208, 0xc0b8aa3b, v198
	v_fmamk_f32 v209, v209, 0xc0b8aa3b, v198
	v_fmamk_f32 v210, v210, 0xc0b8aa3b, v198
	v_fmamk_f32 v211, v211, 0xc0b8aa3b, v198
	v_mul_f32_e32 v204, v204, v132
	v_mul_f32_e32 v205, v205, v133
	v_mul_f32_e32 v206, v206, v134
	v_mul_f32_e32 v207, v207, v135
	v_fma_f32 v132, v200, v208, v204
	v_fma_f32 v133, v201, v209, v205
	v_fma_f32 v134, v202, v210, v206
	v_fma_f32 v135, v203, v211, v207
	v_exp_f32_e32 v200, v132
	v_exp_f32_e32 v201, v133
	v_exp_f32_e32 v202, v134
	v_exp_f32_e32 v203, v135
	v_add_f32_e32 v200, 1.0, v200
	v_add_f32_e32 v201, 1.0, v201
	v_add_f32_e32 v202, 1.0, v202
	v_add_f32_e32 v203, 1.0, v203
	v_rcp_f32_e32 v200, v200
	v_rcp_f32_e32 v201, v201
	v_rcp_f32_e32 v202, v202
	v_rcp_f32_e32 v203, v203
	v_fma_f32 v200, v200, 2.0, -1.0
	v_fma_f32 v201, v201, 2.0, -1.0
	v_fma_f32 v202, v202, 2.0, -1.0
	v_fma_f32 v203, v203, 2.0, -1.0
	v_mul_f32_e32 v216, v212, v200
	v_mul_f32_e32 v217, v213, v201
	v_mul_f32_e32 v218, v214, v202
	v_mul_f32_e32 v219, v215, v203
	v_mul_f32_e32 v236, v216, v228
	v_mul_f32_e32 v237, v216, v232
	v_fmac_f32_e32 v236, v217, v229
	v_fmac_f32_e32 v237, v217, v233
	v_fmac_f32_e32 v236, v218, v230
	v_fmac_f32_e32 v237, v218, v234
	v_fmac_f32_e32 v236, v219, v231
	v_fmac_f32_e32 v237, v219, v235
	v_mov_b32_e32 v238, v236
	v_mov_b32_e32 v239, v236
	v_mov_b32_e32 v240, v237
	v_mov_b32_e32 v241, v237
	s_nop 1
	v_permlane32_swap_b32_e32 v238, v239
	v_permlane32_swap_b32_e32 v240, v241
	v_add_f32_e32 v238, v238, v239
	v_add_f32_e32 v239, v240, v241
	ds_write_b64 v248, v[238:239] offset:256
	v_cvt_pk_f16_f32 v222, v216, v217
	v_cvt_pk_f16_f32 v223, v218, v219
	s_nop 1
	v_permlane32_swap_b32_e32 v220, v222
	v_permlane32_swap_b32_e32 v221, v223
	s_cmp_eq_u32 s31, 0
	s_cbranch_scc1 .LD_slow4
	global_store_dwordx4 v195, v[220:223], s[36:37] offset:0
